# DeltaNet inter-chunk recurrence: half-wave operand transposes by v_permlane32_swap instead of select + ds_bpermute + select (no LDS round trips on the serial chain)
# speedup vs baseline: 1.0074x; 1.0015x over previous
.LBB0_799:
	s_ashr_i32 s4, s16, 1
	s_lshl_b32 s20, s4, 6
	s_and_b32 s17, s4, 3
	s_and_b32 s4, s20, 0xffffff00
	s_or_b32 s14, s4, s17
	s_ashr_i32 s15, s14, 31
	s_lshl_b64 s[4:5], s[14:15], 13
	v_readlane_b32 s6, v253, 22
	v_lshl_add_u64 v[20:21], v[134:135], 0, s[4:5]
	v_readlane_b32 s7, v253, 23
	s_add_u32 s4, s6, s4
	s_addc_u32 s5, s7, s5
	s_lshl_b32 s6, s16, 11
	s_and_b32 s6, s6, 0x800
	v_or_b32_e32 v36, s6, v132
	v_lshlrev_b32_e32 v2, 1, v132
	v_mov_b32_e32 v143, v3
	v_mov_b32_e32 v37, v3
	v_lshlrev_b32_e32 v36, 1, v36
	v_lshl_add_u64 v[16:17], v[20:21], 0, v[2:3]
	v_lshl_add_u64 v[32:33], v[20:21], 0, v[142:143]
	v_mov_b32_e32 v145, v3
	v_lshl_add_u64 v[38:39], s[4:5], 0, v[36:37]
	global_load_dwordx4 v[4:7], v[16:17], off
	global_load_dwordx4 v[8:11], v[16:17], off offset:32
	global_load_dwordx4 v[12:15], v[16:17], off offset:64
	v_lshl_add_u64 v[38:39], v[38:39], 0, v[144:145]
	global_load_dwordx4 v[16:19], v[16:17], off offset:96
	s_nop 0
	global_load_dwordx4 v[20:23], v[32:33], off
	global_load_dwordx4 v[24:27], v[32:33], off offset:32
	global_load_dwordx4 v[28:31], v[32:33], off offset:64
	s_nop 0
	global_load_dwordx4 v[32:35], v[32:33], off offset:96
	s_nop 0
	global_load_dwordx2 v[158:159], v[38:39], off
	global_load_dwordx2 v[154:155], v[38:39], off offset:16
	global_load_dwordx2 v[152:153], v[38:39], off offset:32
	global_load_dwordx2 v[150:151], v[38:39], off offset:48
	global_load_dwordx2 v[164:165], v[38:39], off offset:64
	global_load_dwordx2 v[162:163], v[38:39], off offset:80
	global_load_dwordx2 v[160:161], v[38:39], off offset:96
	global_load_dwordx2 v[156:157], v[38:39], off offset:112
	v_lshl_add_u64 v[146:147], v[138:139], 0, v[36:37]
	v_lshl_add_u64 v[148:149], v[140:141], 0, v[36:37]
	s_mov_b32 s15, 0
	s_waitcnt vmcnt(0)
	v_cndmask_b32_e32 v38, v4, v6, vcc
	ds_bpermute_b32 v38, v166, v38
	s_waitcnt lgkmcnt(0)
	v_cndmask_b32_e32 v92, v38, v4, vcc
	v_mov_b32_e32 v4, 0
	v_mov_b32_e32 v93, v5
	v_mov_b32_e32 v95, v7
	s_nop 1
	v_permlane32_swap_b32_e32 v93, v95
	s_nop 1
	v_cndmask_b32_e32 v94, v6, v38, vcc
	s_waitcnt lgkmcnt(0)
	v_mov_b32_e32 v77, v9
	v_mov_b32_e32 v79, v11
	v_mov_b32_e32 v76, v8
	v_mov_b32_e32 v78, v10
	s_nop 1
	v_permlane32_swap_b32_e32 v77, v79
	v_permlane32_swap_b32_e32 v76, v78
	s_nop 1
	s_waitcnt lgkmcnt(0)
	v_mov_b32_e32 v85, v13
	v_mov_b32_e32 v87, v15
	v_mov_b32_e32 v84, v12
	v_mov_b32_e32 v86, v14
	s_nop 1
	v_permlane32_swap_b32_e32 v85, v87
	v_permlane32_swap_b32_e32 v84, v86
	s_nop 1
	s_waitcnt lgkmcnt(0)
	v_mov_b32_e32 v69, v17
	v_mov_b32_e32 v71, v19
	v_mov_b32_e32 v68, v16
	v_mov_b32_e32 v70, v18
	s_nop 1
	v_permlane32_swap_b32_e32 v69, v71
	v_permlane32_swap_b32_e32 v68, v70
	s_nop 1
	s_waitcnt lgkmcnt(0)
	v_mov_b32_e32 v97, v21
	v_mov_b32_e32 v99, v23
	v_mov_b32_e32 v96, v20
	v_mov_b32_e32 v98, v22
	s_nop 1
	v_permlane32_swap_b32_e32 v97, v99
	v_permlane32_swap_b32_e32 v96, v98
	s_nop 1
	s_waitcnt lgkmcnt(0)
	v_mov_b32_e32 v81, v25
	v_mov_b32_e32 v83, v27
	v_mov_b32_e32 v80, v24
	v_mov_b32_e32 v82, v26
	s_nop 1
	v_permlane32_swap_b32_e32 v81, v83
	v_permlane32_swap_b32_e32 v80, v82
	s_nop 1
	s_waitcnt lgkmcnt(0)
	v_mov_b32_e32 v89, v29
	v_mov_b32_e32 v91, v31
	v_mov_b32_e32 v88, v28
	v_mov_b32_e32 v90, v30
	s_nop 1
	v_permlane32_swap_b32_e32 v89, v91
	v_permlane32_swap_b32_e32 v88, v90
	s_nop 1
	s_waitcnt lgkmcnt(0)
	v_mov_b32_e32 v73, v33
	v_mov_b32_e32 v75, v35
	v_mov_b32_e32 v72, v32
	v_mov_b32_e32 v74, v34
	s_nop 1
	v_permlane32_swap_b32_e32 v73, v75
	v_permlane32_swap_b32_e32 v72, v74
	s_nop 1
	v_mov_b32_e32 v5, v4
	v_mov_b32_e32 v6, v4
	v_mov_b32_e32 v7, v4
	v_mov_b32_e32 v8, v4
	v_mov_b32_e32 v9, v4
	v_mov_b32_e32 v10, v4
	v_mov_b32_e32 v11, v4
	v_mov_b32_e32 v12, v4
	v_mov_b32_e32 v13, v4
	v_mov_b32_e32 v14, v4
	v_mov_b32_e32 v15, v4
	v_mov_b32_e32 v16, v4
	v_mov_b32_e32 v17, v4
	v_mov_b32_e32 v18, v4
	v_mov_b32_e32 v19, v4
	v_mov_b32_e32 v20, v4
	v_mov_b32_e32 v21, v4
	v_mov_b32_e32 v22, v4
	v_mov_b32_e32 v23, v4
	v_mov_b32_e32 v24, v4
	v_mov_b32_e32 v25, v4
	v_mov_b32_e32 v26, v4
	v_mov_b32_e32 v27, v4
	v_mov_b32_e32 v28, v4
	v_mov_b32_e32 v29, v4
	v_mov_b32_e32 v30, v4
	v_mov_b32_e32 v31, v4
	v_mov_b32_e32 v32, v4
	v_mov_b32_e32 v33, v4
	v_mov_b32_e32 v34, v4
	v_mov_b32_e32 v35, v4
.LBB0_800:
	v_lshlrev_b32_e32 v36, 16, v158
	v_and_b32_e32 v37, 0xffff0000, v158
	v_lshlrev_b32_e32 v38, 16, v159
	v_and_b32_e32 v39, 0xffff0000, v159
	v_lshlrev_b32_e32 v40, 16, v154
	v_and_b32_e32 v41, 0xffff0000, v154
	v_lshlrev_b32_e32 v42, 16, v155
	v_and_b32_e32 v43, 0xffff0000, v155
	v_lshlrev_b32_e32 v44, 16, v152
	v_and_b32_e32 v45, 0xffff0000, v152
	v_lshlrev_b32_e32 v46, 16, v153
	v_and_b32_e32 v47, 0xffff0000, v153
	v_lshlrev_b32_e32 v48, 16, v150
	v_and_b32_e32 v49, 0xffff0000, v150
	v_lshlrev_b32_e32 v50, 16, v151
	v_and_b32_e32 v51, 0xffff0000, v151
	v_cvt_pk_bf16_f32 v116, -v20, -v21
	v_cvt_pk_bf16_f32 v117, -v22, -v23
	v_cvt_pk_bf16_f32 v118, -v24, -v25
	v_cvt_pk_bf16_f32 v119, -v26, -v27
	v_lshlrev_b32_e32 v52, 16, v164
	v_and_b32_e32 v53, 0xffff0000, v164
	v_mfma_f32_32x32x16_bf16 v[36:51], v[92:95], v[116:119], v[36:51]
	v_lshlrev_b32_e32 v54, 16, v165
	v_and_b32_e32 v55, 0xffff0000, v165
	v_lshlrev_b32_e32 v56, 16, v162
	v_and_b32_e32 v57, 0xffff0000, v162
	v_lshlrev_b32_e32 v58, 16, v163
	v_and_b32_e32 v59, 0xffff0000, v163
	v_lshlrev_b32_e32 v60, 16, v160
	v_and_b32_e32 v61, 0xffff0000, v160
	v_lshlrev_b32_e32 v62, 16, v161
	v_and_b32_e32 v63, 0xffff0000, v161
	v_lshlrev_b32_e32 v64, 16, v156
	v_and_b32_e32 v65, 0xffff0000, v156
	v_lshlrev_b32_e32 v66, 16, v157
	v_and_b32_e32 v67, 0xffff0000, v157
	s_add_i32 s18, s14, s15
	s_ashr_i32 s19, s18, 31
	v_mfma_f32_32x32x16_bf16 v[52:67], v[96:99], v[116:119], v[52:67]
	s_lshl_b64 s[4:5], s[18:19], 2
	v_cvt_pk_bf16_f32 v120, -v4, -v5
	v_cvt_pk_bf16_f32 v121, -v6, -v7
	v_cvt_pk_bf16_f32 v122, -v8, -v9
	v_cvt_pk_bf16_f32 v123, -v10, -v11
	s_add_u32 s8, s12, s4
	s_addc_u32 s9, s13, s5
	s_lshl_b64 s[6:7], s[18:19], 13
	v_mfma_f32_32x32x16_bf16 v[36:51], v[84:87], v[120:123], v[36:51]
	v_lshl_add_u64 v[96:97], v[136:137], 0, s[6:7]
	v_cvt_pk_bf16_f32 v124, -v28, -v29
	v_cvt_pk_bf16_f32 v125, -v30, -v31
	v_lshl_add_u64 v[150:151], v[96:97], 0, v[2:3]
	v_mfma_f32_32x32x16_bf16 v[52:67], v[88:91], v[120:123], v[52:67]
	v_cvt_pk_bf16_f32 v126, -v32, -v33
	global_load_dword v204, v3, s[8:9]
	v_lshl_add_u64 v[152:153], v[96:97], 0, v[142:143]
	global_load_dwordx4 v[96:99], v[150:151], off
	global_load_dwordx4 v[116:119], v[150:151], off offset:32
	s_add_i32 s4, s18, 4
	s_ashr_i32 s5, s4, 31
	s_lshl_b64 s[4:5], s[4:5], 13
	v_cvt_pk_bf16_f32 v127, -v34, -v35
	global_load_dwordx4 v[84:87], v[152:153], off
	global_load_dwordx4 v[128:131], v[152:153], off offset:32
	global_load_dwordx4 v[168:171], v[150:151], off offset:64
	global_load_dwordx4 v[172:175], v[150:151], off offset:96
	global_load_dwordx4 v[176:179], v[152:153], off offset:64
	global_load_dwordx4 v[180:183], v[152:153], off offset:96
	v_lshl_add_u64 v[150:151], v[134:135], 0, s[4:5]
	v_lshl_add_u64 v[88:89], v[146:147], 0, s[4:5]
	v_cvt_pk_bf16_f32 v92, -v12, -v13
	v_cvt_pk_bf16_f32 v93, -v14, -v15
	v_cvt_pk_bf16_f32 v94, -v16, -v17
	v_cvt_pk_bf16_f32 v95, -v18, -v19
	v_lshl_add_u64 v[120:121], v[150:151], 0, v[2:3]
	v_lshl_add_u64 v[196:197], v[150:151], 0, v[142:143]
	global_load_dwordx2 v[158:159], v[88:89], off
	global_load_dwordx2 v[154:155], v[88:89], off offset:16
	global_load_dwordx2 v[152:153], v[88:89], off offset:32
	v_mfma_f32_32x32x16_bf16 v[36:51], v[76:79], v[124:127], v[36:51]
	global_load_dwordx2 v[150:151], v[88:89], off offset:48
	global_load_dwordx2 v[164:165], v[88:89], off offset:64
	global_load_dwordx2 v[162:163], v[88:89], off offset:80
	global_load_dwordx2 v[160:161], v[88:89], off offset:96
	global_load_dwordx2 v[156:157], v[88:89], off offset:112
	global_load_dwordx4 v[76:79], v[120:121], off
	s_nop 0
	global_load_dwordx4 v[88:91], v[120:121], off offset:32
	v_cvt_pk_bf16_f32 v100, v20, v21
	v_cvt_pk_bf16_f32 v101, v22, v23
	v_cvt_pk_bf16_f32 v102, v4, v5
	v_cvt_pk_bf16_f32 v103, v6, v7
	v_cvt_pk_bf16_f32 v104, v24, v25
	v_cvt_pk_bf16_f32 v105, v26, v27
	v_mfma_f32_32x32x16_bf16 v[52:67], v[80:83], v[124:127], v[52:67]
	global_load_dwordx4 v[80:83], v[120:121], off offset:64
	s_nop 0
	global_load_dwordx4 v[120:123], v[120:121], off offset:96
	s_nop 0
	global_load_dwordx4 v[184:187], v[196:197], off
	global_load_dwordx4 v[188:191], v[196:197], off offset:32
	global_load_dwordx4 v[192:195], v[196:197], off offset:64
	s_nop 0
	global_load_dwordx4 v[196:199], v[196:197], off offset:96
	v_lshl_add_u64 v[206:207], v[148:149], 0, s[6:7]
	v_cvt_pk_bf16_f32 v106, v8, v9
	v_cvt_pk_bf16_f32 v107, v10, v11
	v_cvt_pk_bf16_f32 v108, v28, v29
	v_cvt_pk_bf16_f32 v109, v30, v31
	v_cvt_pk_bf16_f32 v110, v12, v13
	v_mfma_f32_32x32x16_bf16 v[36:51], v[68:71], v[92:95], v[36:51]
	v_cvt_pk_bf16_f32 v111, v14, v15
	v_cvt_pk_bf16_f32 v112, v32, v33
	v_cvt_pk_bf16_f32 v113, v34, v35
	v_cvt_pk_bf16_f32 v114, v16, v17
	v_cvt_pk_bf16_f32 v115, v18, v19
	global_store_dwordx2 v[206:207], v[100:101], off
	global_store_dwordx2 v[206:207], v[102:103], off offset:64
	global_store_dwordx2 v[206:207], v[104:105], off offset:16
	global_store_dwordx2 v[206:207], v[106:107], off offset:80
	global_store_dwordx2 v[206:207], v[108:109], off offset:32
	global_store_dwordx2 v[206:207], v[110:111], off offset:96
	global_store_dwordx2 v[206:207], v[112:113], off offset:48
	global_store_dwordx2 v[206:207], v[114:115], off offset:112
	v_mfma_f32_32x32x16_bf16 v[52:67], v[72:75], v[92:95], v[52:67]
	v_cvt_pk_bf16_f32 v36, v36, v37
	v_cvt_pk_bf16_f32 v37, v38, v39
	v_cvt_pk_bf16_f32 v39, v42, v43
	v_cvt_pk_bf16_f32 v42, v48, v49
	v_cvt_pk_bf16_f32 v38, v40, v41
	v_cvt_pk_bf16_f32 v40, v44, v45
	v_cvt_pk_bf16_f32 v43, v50, v51
	s_nop 4
	v_cvt_pk_bf16_f32 v52, v52, v53
	v_cvt_pk_bf16_f32 v53, v54, v55
	v_cvt_pk_bf16_f32 v54, v56, v57
	v_cvt_pk_bf16_f32 v44, v60, v61
	v_cvt_pk_bf16_f32 v45, v62, v63
	v_cvt_pk_bf16_f32 v41, v46, v47
	v_cvt_pk_bf16_f32 v46, v64, v65
	v_lshl_add_u64 v[208:209], v[146:147], 0, s[6:7]
	v_cvt_pk_bf16_f32 v55, v58, v59
	v_cvt_pk_bf16_f32 v47, v66, v67
	global_store_dwordx2 v[208:209], v[36:37], off
	global_store_dwordx2 v[208:209], v[52:53], off offset:64
	global_store_dwordx2 v[208:209], v[38:39], off offset:16
	global_store_dwordx2 v[208:209], v[54:55], off offset:80
	global_store_dwordx2 v[208:209], v[40:41], off offset:32
	global_store_dwordx2 v[208:209], v[44:45], off offset:96
	global_store_dwordx2 v[208:209], v[42:43], off offset:48
	global_store_dwordx2 v[208:209], v[46:47], off offset:112
	s_add_i32 s15, s15, 4
	s_cmpk_lg_i32 s15, 0xfc
	s_waitcnt vmcnt(40)
	v_pk_mul_f32 v[34:35], v[34:35], v[204:205] op_sel_hi:[1,0]
	s_waitcnt vmcnt(39)
	s_waitcnt vmcnt(38)
	v_pk_mul_f32 v[32:33], v[32:33], v[204:205] op_sel_hi:[1,0]
	v_pk_mul_f32 v[30:31], v[30:31], v[204:205] op_sel_hi:[1,0]
	v_pk_mul_f32 v[28:29], v[28:29], v[204:205] op_sel_hi:[1,0]
	s_waitcnt vmcnt(37)
	s_waitcnt vmcnt(35)
	s_waitcnt vmcnt(34)
	v_pk_mul_f32 v[26:27], v[26:27], v[204:205] op_sel_hi:[1,0]
	v_pk_mul_f32 v[24:25], v[24:25], v[204:205] op_sel_hi:[1,0]
	v_pk_mul_f32 v[22:23], v[22:23], v[204:205] op_sel_hi:[1,0]
	s_waitcnt vmcnt(23)
	v_pk_mul_f32 v[20:21], v[20:21], v[204:205] op_sel_hi:[1,0]
	v_pk_mul_f32 v[18:19], v[18:19], v[204:205] op_sel_hi:[1,0]
	v_pk_mul_f32 v[16:17], v[16:17], v[204:205] op_sel_hi:[1,0]
	s_waitcnt vmcnt(20)
	v_cndmask_b32_e32 v60, v120, v122, vcc
	v_cndmask_b32_e32 v61, v121, v123, vcc
	s_waitcnt vmcnt(19)
	v_cndmask_b32_e32 v62, v184, v186, vcc
	v_cndmask_b32_e32 v63, v185, v187, vcc
	v_pk_mul_f32 v[14:15], v[14:15], v[204:205] op_sel_hi:[1,0]
	v_pk_mul_f32 v[12:13], v[12:13], v[204:205] op_sel_hi:[1,0]
	v_pk_mul_f32 v[10:11], v[10:11], v[204:205] op_sel_hi:[1,0]
	v_pk_mul_f32 v[8:9], v[8:9], v[204:205] op_sel_hi:[1,0]
	v_pk_mul_f32 v[6:7], v[6:7], v[204:205] op_sel_hi:[1,0]
	v_pk_mul_f32 v[4:5], v[4:5], v[204:205] op_sel_hi:[1,0]
	ds_bpermute_b32 v145, v166, v60
	ds_bpermute_b32 v167, v166, v61
	ds_bpermute_b32 v203, v166, v62
	ds_bpermute_b32 v204, v166, v63
	s_waitcnt lgkmcnt(0)
	v_mov_b32_e32 v49, v97
	v_mov_b32_e32 v51, v99
	v_mov_b32_e32 v48, v96
	v_mov_b32_e32 v50, v98
	s_nop 1
	v_permlane32_swap_b32_e32 v49, v51
	v_permlane32_swap_b32_e32 v48, v50
	s_nop 1
	s_waitcnt lgkmcnt(0)
	v_mov_b32_e32 v61, v85
	v_mov_b32_e32 v63, v87
	v_mov_b32_e32 v60, v84
	v_mov_b32_e32 v62, v86
	s_nop 1
	v_permlane32_swap_b32_e32 v61, v63
	v_permlane32_swap_b32_e32 v60, v62
	s_nop 1
	v_mfma_f32_32x32x16_bf16 v[20:35], v[48:51], v[36:39], v[20:35]
	s_waitcnt lgkmcnt(0)
	v_mov_b32_e32 v49, v169
	v_mov_b32_e32 v51, v171
	v_mov_b32_e32 v48, v168
	v_mov_b32_e32 v50, v170
	s_nop 1
	v_permlane32_swap_b32_e32 v49, v51
	v_permlane32_swap_b32_e32 v48, v50
	s_nop 1
	v_mfma_f32_32x32x16_bf16 v[4:19], v[60:63], v[36:39], v[4:19]
	s_waitcnt lgkmcnt(0)
	v_mov_b32_e32 v37, v177
	v_mov_b32_e32 v39, v179
	v_mov_b32_e32 v36, v176
	v_mov_b32_e32 v38, v178
	s_nop 1
	v_permlane32_swap_b32_e32 v37, v39
	v_permlane32_swap_b32_e32 v36, v38
	s_nop 1
	v_mfma_f32_32x32x16_bf16 v[20:35], v[48:51], v[52:55], v[20:35]
	s_waitcnt vmcnt(18)
	v_cndmask_b32_e32 v64, v188, v190, vcc
	v_mfma_f32_32x32x16_bf16 v[4:19], v[36:39], v[52:55], v[4:19]
	v_cndmask_b32_e32 v65, v189, v191, vcc
	s_waitcnt vmcnt(17)
	ds_bpermute_b32 v205, v166, v64
	ds_bpermute_b32 v206, v166, v65
	v_mov_b32_e32 v57, v117
	v_mov_b32_e32 v59, v119
	v_mov_b32_e32 v56, v116
	v_mov_b32_e32 v58, v118
	s_nop 1
	v_permlane32_swap_b32_e32 v57, v59
	v_permlane32_swap_b32_e32 v56, v58
	s_nop 1
	s_waitcnt lgkmcnt(0)
	v_mov_b32_e32 v65, v129
	v_mov_b32_e32 v67, v131
	v_mov_b32_e32 v64, v128
	v_mov_b32_e32 v66, v130
	s_nop 1
	v_permlane32_swap_b32_e32 v65, v67
	v_permlane32_swap_b32_e32 v64, v66
	s_nop 1
	v_mfma_f32_32x32x16_bf16 v[20:35], v[56:59], v[40:43], v[20:35]
	v_mov_b32_e32 v69, v173
	v_mov_b32_e32 v71, v175
	v_mov_b32_e32 v68, v172
	v_mov_b32_e32 v70, v174
	s_nop 1
	v_permlane32_swap_b32_e32 v69, v71
	v_permlane32_swap_b32_e32 v68, v70
	s_nop 1
	s_waitcnt lgkmcnt(0)
	v_mov_b32_e32 v61, v181
	v_mov_b32_e32 v63, v183
	v_mov_b32_e32 v60, v180
	v_mov_b32_e32 v62, v182
	s_nop 1
	v_permlane32_swap_b32_e32 v61, v63
	v_permlane32_swap_b32_e32 v60, v62
	s_nop 1
	v_mfma_f32_32x32x16_bf16 v[4:19], v[64:67], v[40:43], v[4:19]
	s_waitcnt vmcnt(16)
	v_mov_b32_e32 v129, v77
	v_mov_b32_e32 v131, v79
	v_mov_b32_e32 v128, v76
	v_mov_b32_e32 v130, v78
	s_nop 1
	v_permlane32_swap_b32_e32 v129, v131
	v_permlane32_swap_b32_e32 v128, v130
	s_nop 1
	v_mfma_f32_32x32x16_bf16 v[20:35], v[68:71], v[44:47], v[20:35]
	s_waitcnt lgkmcnt(0)
	v_mov_b32_e32 v113, v89
	v_mov_b32_e32 v115, v91
	v_mov_b32_e32 v112, v88
	v_mov_b32_e32 v114, v90
	s_nop 1
	v_permlane32_swap_b32_e32 v113, v115
	v_permlane32_swap_b32_e32 v112, v114
	s_nop 1
	s_waitcnt lgkmcnt(0)
	v_mov_b32_e32 v125, v81
	v_mov_b32_e32 v127, v83
	v_mov_b32_e32 v124, v80
	v_mov_b32_e32 v126, v82
	s_nop 1
	v_permlane32_swap_b32_e32 v125, v127
	v_permlane32_swap_b32_e32 v124, v126
	s_nop 1
	v_mfma_f32_32x32x16_bf16 v[4:19], v[60:63], v[44:47], v[4:19]
	v_cndmask_b32_e32 v109, v167, v121, vcc
	v_cndmask_b32_e32 v108, v145, v120, vcc
	v_cndmask_b32_e32 v121, v204, v185, vcc
	v_cndmask_b32_e32 v120, v203, v184, vcc
	s_waitcnt lgkmcnt(0)
	v_cndmask_b32_e32 v105, v206, v189, vcc
	v_cndmask_b32_e32 v104, v205, v188, vcc
	s_waitcnt lgkmcnt(0)
	v_mov_b32_e32 v117, v193
	v_mov_b32_e32 v119, v195
	v_mov_b32_e32 v116, v192
	v_mov_b32_e32 v118, v194
	s_nop 1
	v_permlane32_swap_b32_e32 v117, v119
	v_permlane32_swap_b32_e32 v116, v118
	s_nop 1
	s_waitcnt lgkmcnt(0)
	v_mov_b32_e32 v101, v197
	v_mov_b32_e32 v103, v199
	v_mov_b32_e32 v100, v196
	v_mov_b32_e32 v102, v198
	s_nop 1
	v_permlane32_swap_b32_e32 v101, v103
	v_permlane32_swap_b32_e32 v100, v102
	s_nop 1
	v_cndmask_b32_e32 v111, v123, v167, vcc
	v_cndmask_b32_e32 v110, v122, v145, vcc
	v_cndmask_b32_e32 v123, v187, v204, vcc
	v_cndmask_b32_e32 v122, v186, v203, vcc
	v_cndmask_b32_e32 v107, v191, v206, vcc
	v_cndmask_b32_e32 v106, v190, v205, vcc
	v_mov_b64_e32 v[72:73], v[100:101]
	v_mov_b64_e32 v[88:89], v[116:117]
	v_mov_b64_e32 v[80:81], v[104:105]
	v_mov_b64_e32 v[96:97], v[120:121]
	v_mov_b64_e32 v[68:69], v[108:109]
	v_mov_b64_e32 v[84:85], v[124:125]
	v_mov_b64_e32 v[76:77], v[112:113]
	v_mov_b64_e32 v[92:93], v[128:129]
	v_mov_b64_e32 v[74:75], v[102:103]
	v_mov_b64_e32 v[90:91], v[118:119]
	v_mov_b64_e32 v[82:83], v[106:107]
	v_mov_b64_e32 v[98:99], v[122:123]
	v_mov_b64_e32 v[70:71], v[110:111]
	v_mov_b64_e32 v[86:87], v[126:127]
	v_mov_b64_e32 v[78:79], v[114:115]
	v_mov_b64_e32 v[94:95], v[130:131]
	s_cbranch_scc1 .LBB0_800
	v_cvt_pk_bf16_f32 v70, v20, v21
	v_cvt_pk_bf16_f32 v20, -v20, -v21
	v_cvt_pk_bf16_f32 v71, v22, v23
	v_cvt_pk_bf16_f32 v21, -v22, -v23
	v_cvt_pk_bf16_f32 v22, -v24, -v25
	v_lshlrev_b32_e32 v52, 16, v158
	v_and_b32_e32 v53, 0xffff0000, v158
	v_lshlrev_b32_e32 v54, 16, v159
	v_and_b32_e32 v55, 0xffff0000, v159
	v_lshlrev_b32_e32 v56, 16, v154
	v_and_b32_e32 v57, 0xffff0000, v154
	v_lshlrev_b32_e32 v58, 16, v155
	v_and_b32_e32 v59, 0xffff0000, v155
	v_lshlrev_b32_e32 v60, 16, v152
	v_and_b32_e32 v61, 0xffff0000, v152
	v_lshlrev_b32_e32 v62, 16, v153
	v_and_b32_e32 v63, 0xffff0000, v153
	v_lshlrev_b32_e32 v64, 16, v150
	v_and_b32_e32 v65, 0xffff0000, v150
	v_lshlrev_b32_e32 v66, 16, v151
	v_and_b32_e32 v67, 0xffff0000, v151
	v_cvt_pk_bf16_f32 v23, -v26, -v27
	v_lshlrev_b32_e32 v36, 16, v164
	v_and_b32_e32 v37, 0xffff0000, v164
	v_lshlrev_b32_e32 v38, 16, v165
	v_and_b32_e32 v39, 0xffff0000, v165
	v_lshlrev_b32_e32 v40, 16, v162
	v_and_b32_e32 v41, 0xffff0000, v162
	v_lshlrev_b32_e32 v42, 16, v163
	v_and_b32_e32 v43, 0xffff0000, v163
	v_lshlrev_b32_e32 v44, 16, v160
	v_and_b32_e32 v45, 0xffff0000, v160
	v_lshlrev_b32_e32 v46, 16, v161
	v_and_b32_e32 v47, 0xffff0000, v161
	v_lshlrev_b32_e32 v48, 16, v156
	v_and_b32_e32 v49, 0xffff0000, v156
	v_lshlrev_b32_e32 v50, 16, v157
	v_and_b32_e32 v51, 0xffff0000, v157
	v_mfma_f32_32x32x16_bf16 v[52:67], v[128:131], v[20:23], v[52:67]
	v_cvt_pk_bf16_f32 v72, v4, v5
	v_cvt_pk_bf16_f32 v4, -v4, -v5
	v_cvt_pk_bf16_f32 v73, v6, v7
	v_mfma_f32_32x32x16_bf16 v[36:51], v[120:123], v[20:23], v[36:51]
	v_cvt_pk_bf16_f32 v5, -v6, -v7
	v_cvt_pk_bf16_f32 v6, -v8, -v9
	v_cvt_pk_bf16_f32 v7, -v10, -v11
	s_or_b32 s4, s20, s17
	v_mfma_f32_32x32x16_bf16 v[52:67], v[124:127], v[4:7], v[52:67]
	s_or_b32 s4, s4, 0xfc
	s_ashr_i32 s5, s4, 31
	s_lshl_b64 s[14:15], s[4:5], 13
	v_lshl_add_u64 v[68:69], v[148:149], 0, s[14:15]
	global_store_dwordx2 v[68:69], v[70:71], off
	global_store_dwordx2 v[68:69], v[72:73], off offset:64
	v_cvt_pk_bf16_f32 v72, v8, v9
	v_mfma_f32_32x32x16_bf16 v[36:51], v[116:119], v[4:7], v[36:51]
	v_cvt_pk_bf16_f32 v4, -v28, -v29
	v_cvt_pk_bf16_f32 v5, -v30, -v31
	v_cvt_pk_bf16_f32 v6, -v32, -v33
	v_cvt_pk_bf16_f32 v7, -v34, -v35
	v_cvt_pk_bf16_f32 v8, -v12, -v13
	v_mfma_f32_32x32x16_bf16 v[52:67], v[112:115], v[4:7], v[52:67]
	v_cvt_pk_bf16_f32 v73, v10, v11
	v_cvt_pk_bf16_f32 v9, -v14, -v15
	v_cvt_pk_bf16_f32 v10, -v16, -v17
	v_mfma_f32_32x32x16_bf16 v[36:51], v[104:107], v[4:7], v[36:51]
	v_xor_b32_e32 v2, 0x80000000, v18
	v_xor_b32_e32 v11, 0x80000000, v19
	v_cvt_pk_bf16_f32 v11, v2, v11
	v_cvt_pk_bf16_f32 v70, v24, v25
	v_cvt_pk_bf16_f32 v71, v26, v27
	global_store_dwordx2 v[68:69], v[70:71], off offset:16
	global_store_dwordx2 v[68:69], v[72:73], off offset:80
	v_cvt_pk_bf16_f32 v70, v28, v29
	v_mfma_f32_32x32x16_bf16 v[52:67], v[108:111], v[8:11], v[52:67]
	v_cvt_pk_bf16_f32 v71, v30, v31
	v_cvt_pk_bf16_f32 v72, v12, v13
	v_cvt_pk_bf16_f32 v73, v14, v15
	global_store_dwordx2 v[68:69], v[70:71], off offset:32
	global_store_dwordx2 v[68:69], v[72:73], off offset:96
	v_cvt_pk_bf16_f32 v70, v32, v33
	v_cvt_pk_bf16_f32 v71, v34, v35
	v_lshl_add_u64 v[4:5], v[146:147], 0, s[14:15]
	v_mfma_f32_32x32x16_bf16 v[36:51], v[100:103], v[8:11], v[36:51]
	s_nop 2
	v_cvt_pk_bf16_f32 v6, v52, v53
	v_cvt_pk_bf16_f32 v7, v54, v55
	v_cvt_pk_bf16_f32 v72, v16, v17
	v_cvt_pk_bf16_f32 v73, v18, v19
	global_store_dwordx2 v[68:69], v[70:71], off offset:48
	global_store_dwordx2 v[68:69], v[72:73], off offset:112
	s_add_i32 s16, s16, s54
	s_cmp_lt_i32 s16, 64
	s_nop 0
	v_cvt_pk_bf16_f32 v8, v36, v37
	v_cvt_pk_bf16_f32 v9, v38, v39
	global_store_dwordx2 v[4:5], v[6:7], off
	global_store_dwordx2 v[4:5], v[8:9], off offset:64
	v_cvt_pk_bf16_f32 v6, v56, v57
	v_cvt_pk_bf16_f32 v7, v58, v59
	v_cvt_pk_bf16_f32 v8, v40, v41
	v_cvt_pk_bf16_f32 v9, v42, v43
	global_store_dwordx2 v[4:5], v[6:7], off offset:16
	global_store_dwordx2 v[4:5], v[8:9], off offset:80
	v_cvt_pk_bf16_f32 v6, v60, v61
	v_cvt_pk_bf16_f32 v7, v62, v63
	v_cvt_pk_bf16_f32 v8, v44, v45
	v_cvt_pk_bf16_f32 v9, v46, v47
	global_store_dwordx2 v[4:5], v[6:7], off offset:32
	global_store_dwordx2 v[4:5], v[8:9], off offset:96
	v_cvt_pk_bf16_f32 v6, v64, v65
	v_cvt_pk_bf16_f32 v7, v66, v67
	v_cvt_pk_bf16_f32 v8, v48, v49
	v_cvt_pk_bf16_f32 v9, v50, v51
	global_store_dwordx2 v[4:5], v[6:7], off offset:48
	global_store_dwordx2 v[4:5], v[8:9], off offset:112
	s_cbranch_scc1 .LBB0_799
